# SGU: late stats loads and post-barrier transpose loads hoisted to the unit top (register copies at the old load sites), counted vmcnt
# speedup vs baseline: 1.0082x; 1.0024x over previous
; #define LAS __attribute__((address_space(3)))
; __device__ __forceinline__ bf16 f2bf(float f) { return (bf16)cvt_pk_bf16(f, f); }
; template <int PH, bool PRB = false>
; __device__ __forceinline__ void run_phase(int layer, LAS unsigned char* lds, const int wv_) {
;     ...
;             u32x4 vw[4];
; #pragma unroll
;             for (int it = 0; it < 4; ++it) { const int item = tid + NT * it; vw[it] = *(const u32x4*)(z + (size_t)(t0 + (item & 127)) * EVEN_IN + 512 + g * 128 + 8 * (item >> 7)); }
; #pragma unroll
;             for (int it = 0; it < 4; ++it) {
;                 const int item = tid + NT * it, q = item & 127, cc = item >> 7;
;                 const u32x4 w = vw[it]; const float mu = st[2 * q], rstd = st[2 * q + 1];
; #pragma unroll
;                 for (int k = 0; k < 8; ++k) { const int c = 8 * cc + k; const float v = (k & 1) ? __uint_as_float(w[k >> 1] & 0xffff0000u) : __uint_as_float(w[k >> 1] << 16);
;                     *(LAS bf16*)(vnt + c * 272 + q * 2) = f2bf((v - mu) * rstd * lg[g * 128 + c] + lb[g * 128 + c]); }
;             }
.LBB0_639:
	s_or_b64 exec, exec, s[12:13]
	s_waitcnt lgkmcnt(0)
	v_or_b32_e32 v2, s18, v116
	v_mov_b64_e32 v[0:1], s[2:3]
	v_mad_i64_i32 v[0:1], s[4:5], v2, s60, v[0:1]
	s_lshl_b32 s50, s19, 1
	v_lshl_add_u64 v[0:1], v[0:1], 0, s[50:51]
	v_lshl_add_u64 v[2:3], v[62:63], 1, v[0:1]
	s_barrier
	v_mov_b64_e32 v[12:13], v[230:231]
	v_mov_b64_e32 v[14:15], v[232:233]
	v_add_u32_e32 v2, s19, v62
	v_ashrrev_i32_e32 v3, 31, v2
	v_lshlrev_b64 v[2:3], 2, v[2:3]
	v_lshl_add_u64 v[20:21], s[6:7], 0, v[2:3]
	v_lshl_add_u64 v[22:23], s[8:9], 0, v[2:3]
	global_load_dword v26, v[20:21], off
	global_load_dword v27, v[22:23], off
	ds_read_b64 v[24:25], v117
	v_lshl_add_u64 v[2:3], v[66:67], 1, v[0:1]
	v_lshl_add_u64 v[4:5], v[68:69], 1, v[0:1]
	v_lshl_add_u64 v[0:1], v[70:71], 1, v[0:1]
	v_mov_b64_e32 v[8:9], v[234:235]
	v_mov_b64_e32 v[10:11], v[236:237]
	s_nop 0
	v_mov_b64_e32 v[4:5], v[238:239]
	v_mov_b64_e32 v[6:7], v[240:241]
	s_nop 0
	v_mov_b64_e32 v[0:1], v[246:247]
	v_mov_b64_e32 v[2:3], v[248:249]
	global_load_dwordx4 v[188:191], v[20:21], off
	global_load_dwordx4 v[196:199], v[22:23], off
	global_load_dwordx4 v[192:195], v[20:21], off offset:16
	global_load_dwordx4 v[200:203], v[22:23], off offset:16
	global_load_dwordx4 v[204:207], v[20:21], off offset:128
	global_load_dwordx4 v[212:215], v[22:23], off offset:128
	global_load_dwordx4 v[208:211], v[20:21], off offset:144
	global_load_dwordx4 v[222:225], v[22:23], off offset:144
	global_load_dwordx4 v[230:233], v[20:21], off offset:256
	global_load_dwordx4 v[238:241], v[22:23], off offset:256
	global_load_dwordx4 v[234:237], v[20:21], off offset:272
	global_load_dwordx4 v[246:249], v[22:23], off offset:272
	s_waitcnt vmcnt(0) lgkmcnt(0)
	v_lshlrev_b32_e32 v216, 16, v12
	v_sub_f32_e32 v216, v216, v24
	v_mul_f32_e32 v216, v25, v216
	v_fmac_f32_e32 v196, v188, v216
	v_cvt_pk_bf16_f32 v196, v196, v196
	ds_write_b16 v141, v196
	v_and_b32_e32 v217, 0xffff0000, v12
	v_sub_f32_e32 v217, v217, v24
	v_mul_f32_e32 v217, v25, v217
	v_fmac_f32_e32 v197, v189, v217
	v_cvt_pk_bf16_f32 v197, v197, v197
	ds_write_b16 v141, v197 offset:272
	v_lshlrev_b32_e32 v216, 16, v13
	v_sub_f32_e32 v216, v216, v24
	v_mul_f32_e32 v216, v25, v216
	v_fmac_f32_e32 v198, v190, v216
	v_cvt_pk_bf16_f32 v198, v198, v198
	ds_write_b16 v141, v198 offset:544
	v_and_b32_e32 v217, 0xffff0000, v13
	v_sub_f32_e32 v217, v217, v24
	v_mul_f32_e32 v217, v25, v217
	v_fmac_f32_e32 v199, v191, v217
	v_cvt_pk_bf16_f32 v199, v199, v199
	ds_write_b16 v141, v199 offset:816
	v_lshlrev_b32_e32 v216, 16, v14
	v_sub_f32_e32 v216, v216, v24
	v_mul_f32_e32 v216, v25, v216
	v_fmac_f32_e32 v200, v192, v216
	v_cvt_pk_bf16_f32 v200, v200, v200
	ds_write_b16 v141, v200 offset:1088
	v_and_b32_e32 v217, 0xffff0000, v14
	v_sub_f32_e32 v217, v217, v24
	v_mul_f32_e32 v217, v25, v217
	v_fmac_f32_e32 v201, v193, v217
	v_cvt_pk_bf16_f32 v201, v201, v201
	ds_write_b16 v141, v201 offset:1360
	v_lshlrev_b32_e32 v216, 16, v15
	v_sub_f32_e32 v216, v216, v24
	v_mul_f32_e32 v216, v25, v216
	v_fmac_f32_e32 v202, v194, v216
	v_cvt_pk_bf16_f32 v202, v202, v202
	ds_write_b16 v141, v202 offset:1632
	v_and_b32_e32 v217, 0xffff0000, v15
	v_sub_f32_e32 v217, v217, v24
	v_mul_f32_e32 v217, v25, v217
	v_fmac_f32_e32 v203, v195, v217
	v_cvt_pk_bf16_f32 v203, v203, v203
	ds_write_b16 v142, v203
	global_load_dwordx4 v[188:191], v[20:21], off offset:384
	global_load_dwordx4 v[196:199], v[22:23], off offset:384
	global_load_dwordx4 v[192:195], v[20:21], off offset:400
	global_load_dwordx4 v[200:203], v[22:23], off offset:400
	v_lshlrev_b32_e32 v216, 16, v8
	v_sub_f32_e32 v216, v216, v24
	v_mul_f32_e32 v216, v25, v216
	v_fmac_f32_e32 v212, v204, v216
	v_cvt_pk_bf16_f32 v212, v212, v212
	ds_write_b16 v143, v212
	v_and_b32_e32 v217, 0xffff0000, v8
	v_sub_f32_e32 v217, v217, v24
	v_mul_f32_e32 v217, v25, v217
	v_fmac_f32_e32 v213, v205, v217
	v_cvt_pk_bf16_f32 v213, v213, v213
	ds_write_b16 v143, v213 offset:272
	v_lshlrev_b32_e32 v216, 16, v9
	v_sub_f32_e32 v216, v216, v24
	v_mul_f32_e32 v216, v25, v216
	v_fmac_f32_e32 v214, v206, v216
	v_cvt_pk_bf16_f32 v214, v214, v214
	ds_write_b16 v143, v214 offset:544
	v_and_b32_e32 v217, 0xffff0000, v9
	v_sub_f32_e32 v217, v217, v24
	v_mul_f32_e32 v217, v25, v217
	v_fmac_f32_e32 v215, v207, v217
	v_cvt_pk_bf16_f32 v215, v215, v215
	ds_write_b16 v143, v215 offset:816
	v_lshlrev_b32_e32 v216, 16, v10
	v_sub_f32_e32 v216, v216, v24
	v_mul_f32_e32 v216, v25, v216
	v_fmac_f32_e32 v222, v208, v216
	v_cvt_pk_bf16_f32 v222, v222, v222
	ds_write_b16 v143, v222 offset:1088
	v_and_b32_e32 v217, 0xffff0000, v10
	v_sub_f32_e32 v217, v217, v24
	v_mul_f32_e32 v217, v25, v217
	v_fmac_f32_e32 v223, v209, v217
	v_cvt_pk_bf16_f32 v223, v223, v223
	ds_write_b16 v143, v223 offset:1360
	v_lshlrev_b32_e32 v216, 16, v11
	v_sub_f32_e32 v216, v216, v24
	v_mul_f32_e32 v216, v25, v216
	v_fmac_f32_e32 v224, v210, v216
	v_cvt_pk_bf16_f32 v224, v224, v224
	ds_write_b16 v143, v224 offset:1632
	v_and_b32_e32 v217, 0xffff0000, v11
	v_sub_f32_e32 v217, v217, v24
	v_mul_f32_e32 v217, v25, v217
	v_fmac_f32_e32 v225, v211, v217
	v_cvt_pk_bf16_f32 v225, v225, v225
	ds_write_b16 v144, v225
	v_lshlrev_b32_e32 v216, 16, v4
	v_sub_f32_e32 v216, v216, v24
	v_mul_f32_e32 v216, v25, v216
	v_fmac_f32_e32 v238, v230, v216
	v_cvt_pk_bf16_f32 v238, v238, v238
	ds_write_b16 v145, v238
	v_and_b32_e32 v217, 0xffff0000, v4
	v_sub_f32_e32 v217, v217, v24
	v_mul_f32_e32 v217, v25, v217
	v_fmac_f32_e32 v239, v231, v217
	v_cvt_pk_bf16_f32 v239, v239, v239
	ds_write_b16 v145, v239 offset:272
	v_lshlrev_b32_e32 v216, 16, v5
	v_sub_f32_e32 v216, v216, v24
	v_mul_f32_e32 v216, v25, v216
	v_fmac_f32_e32 v240, v232, v216
	v_cvt_pk_bf16_f32 v240, v240, v240
	ds_write_b16 v145, v240 offset:544
	v_and_b32_e32 v217, 0xffff0000, v5
	v_sub_f32_e32 v217, v217, v24
	v_mul_f32_e32 v217, v25, v217
	v_fmac_f32_e32 v241, v233, v217
	v_cvt_pk_bf16_f32 v241, v241, v241
	ds_write_b16 v145, v241 offset:816
	v_lshlrev_b32_e32 v216, 16, v6
	v_sub_f32_e32 v216, v216, v24
	v_mul_f32_e32 v216, v25, v216
	v_fmac_f32_e32 v246, v234, v216
	v_cvt_pk_bf16_f32 v246, v246, v246
	ds_write_b16 v145, v246 offset:1088
	v_and_b32_e32 v217, 0xffff0000, v6
	v_sub_f32_e32 v217, v217, v24
	v_mul_f32_e32 v217, v25, v217
	v_fmac_f32_e32 v247, v235, v217
	v_cvt_pk_bf16_f32 v247, v247, v247
	ds_write_b16 v145, v247 offset:1360
	v_lshlrev_b32_e32 v216, 16, v7
	v_sub_f32_e32 v216, v216, v24
	v_mul_f32_e32 v216, v25, v216
	v_fmac_f32_e32 v248, v236, v216
	v_cvt_pk_bf16_f32 v248, v248, v248
	ds_write_b16 v145, v248 offset:1632
	v_and_b32_e32 v217, 0xffff0000, v7
	v_sub_f32_e32 v217, v217, v24
	v_mul_f32_e32 v217, v25, v217
	v_fmac_f32_e32 v249, v237, v217
	v_cvt_pk_bf16_f32 v249, v249, v249
	ds_write_b16 v146, v249
	s_waitcnt vmcnt(0)
; #define LAS __attribute__((address_space(3)))
; __device__ __forceinline__ bf16 f2bf(float f) { return (bf16)cvt_pk_bf16(f, f); }
; __device__ __forceinline__ int crow(int r, int hi) { return (r & 3) + 8 * (r >> 2) + 4 * hi; }
; template <int PH, bool PRB = false>
; __device__ __forceinline__ void run_phase(int layer, LAS unsigned char* lds, const int wv_) {
;     ...
;             for (int it = 0; it < 4; ++it) {
;                 const int item = tid + NT * it, q = item & 127, cc = item >> 7;
;                 const u32x4 w = vw[it]; const float mu = st[2 * q], rstd = st[2 * q + 1];
; #pragma unroll
;                 for (int k = 0; k < 8; ++k) { const int c = 8 * cc + k; const float v = (k & 1) ? __uint_as_float(w[k >> 1] & 0xffff0000u) : __uint_as_float(w[k >> 1] << 16);
;                     *(LAS bf16*)(vnt + c * 272 + q * 2) = f2bf((v - mu) * rstd * lg[g * 128 + c] + lb[g * 128 + c]); }
;             }
;     ...
;                 const int col = g * 128 + 32 * cb0 + r32; bf16 u0[16], u1[16]; float bias[16];
; #pragma unroll
;                 for (int r = 0; r < 16; ++r) { const int prow = 32 * pb + att::crow(r, hi), tok = t0 + prow; bias[r] = bs[g * 128 + prow];
;                     u0[r] = z[(size_t)tok * EVEN_IN + col]; u1[r] = z[(size_t)tok * EVEN_IN + col + 32]; }
; #pragma unroll
;                 for (int r = 0; r < 16; ++r) { const int tok = t0 + 32 * pb + att::crow(r, hi);
	v_lshlrev_b32_e32 v216, 16, v0
	v_sub_f32_e32 v216, v216, v24
	v_mul_f32_e32 v216, v25, v216
	v_fmac_f32_e32 v196, v188, v216
	v_cvt_pk_bf16_f32 v196, v196, v196
	ds_write_b16 v147, v196
	v_and_b32_e32 v217, 0xffff0000, v0
	v_sub_f32_e32 v217, v217, v24
	v_mul_f32_e32 v217, v25, v217
	v_fmac_f32_e32 v197, v189, v217
	v_cvt_pk_bf16_f32 v197, v197, v197
	ds_write_b16 v147, v197 offset:272
	v_lshlrev_b32_e32 v216, 16, v1
	v_sub_f32_e32 v216, v216, v24
	v_mul_f32_e32 v216, v25, v216
	v_fmac_f32_e32 v198, v190, v216
	v_cvt_pk_bf16_f32 v198, v198, v198
	ds_write_b16 v147, v198 offset:544
	v_and_b32_e32 v217, 0xffff0000, v1
	v_sub_f32_e32 v217, v217, v24
	v_mul_f32_e32 v217, v25, v217
	v_fmac_f32_e32 v199, v191, v217
	v_cvt_pk_bf16_f32 v199, v199, v199
	ds_write_b16 v147, v199 offset:816
	v_lshlrev_b32_e32 v216, 16, v2
	v_sub_f32_e32 v216, v216, v24
	v_mul_f32_e32 v216, v25, v216
	v_fmac_f32_e32 v200, v192, v216
	v_cvt_pk_bf16_f32 v200, v200, v200
	ds_write_b16 v147, v200 offset:1088
	v_and_b32_e32 v217, 0xffff0000, v2
	v_sub_f32_e32 v217, v217, v24
	v_mul_f32_e32 v217, v25, v217
	v_fmac_f32_e32 v201, v193, v217
	v_cvt_pk_bf16_f32 v201, v201, v201
	ds_write_b16 v147, v201 offset:1360
	v_lshlrev_b32_e32 v216, 16, v3
	v_sub_f32_e32 v216, v216, v24
	v_mul_f32_e32 v216, v25, v216
	v_fmac_f32_e32 v202, v194, v216
	v_cvt_pk_bf16_f32 v202, v202, v202
	ds_write_b16 v147, v202 offset:1632
	v_and_b32_e32 v217, 0xffff0000, v3
	v_sub_f32_e32 v217, v217, v24
	v_mul_f32_e32 v217, v25, v217
	v_fmac_f32_e32 v203, v195, v217
	v_cvt_pk_bf16_f32 v203, v203, v203
	ds_write_b16 v148, v203
	s_and_b32 s4, s14, 0x7fffffc
	s_add_i32 s4, s4, s15
	v_lshl_or_b32 v96, s4, 5, v119
	v_add_u32_e32 v29, s18, v139
	v_readlane_b32 s5, v254, 20
	v_ashrrev_i32_e32 v97, 31, v96
	s_add_i32 s16, s16, s5
	v_or_b32_e32 v110, 1, v96
	v_or_b32_e32 v112, 2, v96
	v_or_b32_e32 v150, 3, v96
	v_or_b32_e32 v152, 8, v96
	v_or_b32_e32 v160, 9, v96
	v_or_b32_e32 v162, 10, v96
	v_or_b32_e32 v164, 11, v96
	v_or_b32_e32 v166, 16, v96
	v_or_b32_e32 v168, 17, v96
	v_or_b32_e32 v170, 18, v96
	v_or_b32_e32 v172, 19, v96
	v_or_b32_e32 v174, 24, v96
	v_or_b32_e32 v176, 25, v96
	v_or_b32_e32 v178, 26, v96
	v_or_b32_e32 v106, 27, v96
	v_lshlrev_b64 v[180:181], 11, v[96:97]
	v_ashrrev_i32_e32 v151, 31, v150
	v_ashrrev_i32_e32 v153, 31, v152
	v_lshlrev_b64 v[184:185], 11, v[150:151]
	v_lshlrev_b64 v[186:187], 11, v[152:153]
	v_ashrrev_i32_e32 v111, 31, v110
	v_ashrrev_i32_e32 v161, 31, v160
	v_ashrrev_i32_e32 v163, 31, v162
	v_ashrrev_i32_e32 v165, 31, v164
	v_ashrrev_i32_e32 v167, 31, v166
	v_ashrrev_i32_e32 v113, 31, v112
	v_ashrrev_i32_e32 v169, 31, v168
	v_lshlrev_b64 v[182:183], 11, v[112:113]
	v_lshlrev_b64 v[112:113], 11, v[168:169]
	v_ashrrev_i32_e32 v171, 31, v170
	v_ashrrev_i32_e32 v173, 31, v172
	v_ashrrev_i32_e32 v107, 31, v106
	v_ashrrev_i32_e32 v175, 31, v174
	v_ashrrev_i32_e32 v177, 31, v176
	v_ashrrev_i32_e32 v179, 31, v178
	s_add_i32 s14, s14, s95
	s_add_i32 s17, s17, s81
	s_cmpk_lt_i32 s14, 0x200
	v_add_u32_e32 v28, s18, v138
	v_add_u32_e32 v12, s19, v121
	v_add_u32_e32 v27, s18, v137
	s_nop 0
	v_ashrrev_i32_e32 v13, 31, v12
	v_lshlrev_b64 v[12:13], 2, v[12:13]
	v_lshl_add_u64 v[20:21], s[6:7], 0, v[12:13]
	v_lshl_add_u64 v[12:13], s[8:9], 0, v[12:13]
	v_add_u32_e32 v12, s19, v66
	v_ashrrev_i32_e32 v13, 31, v12
	v_lshlrev_b64 v[12:13], 2, v[12:13]
	v_lshl_add_u64 v[20:21], s[6:7], 0, v[12:13]
	v_lshl_add_u64 v[12:13], s[8:9], 0, v[12:13]
	v_add_u32_e32 v26, s18, v136
	ds_read_b64 v[14:15], v117
	v_add_u32_e32 v25, s18, v135
	v_add_u32_e32 v24, s18, v134
	v_add_u32_e32 v8, s19, v122
	v_add_u32_e32 v23, s18, v133
	s_nop 0
	v_ashrrev_i32_e32 v9, 31, v8
	v_lshlrev_b64 v[8:9], 2, v[8:9]
	v_lshl_add_u64 v[12:13], s[6:7], 0, v[8:9]
	v_lshl_add_u64 v[8:9], s[8:9], 0, v[8:9]
	v_add_u32_e32 v8, s19, v68
	v_ashrrev_i32_e32 v9, 31, v8
	v_lshlrev_b64 v[8:9], 2, v[8:9]
	v_lshl_add_u64 v[12:13], s[6:7], 0, v[8:9]
	v_lshl_add_u64 v[8:9], s[8:9], 0, v[8:9]
	v_add_u32_e32 v22, s18, v132
	ds_read_b64 v[10:11], v117
	v_add_u32_e32 v21, s18, v131
	v_add_u32_e32 v20, s18, v130
	v_add_u32_e32 v4, s19, v123
	s_nop 0
	v_ashrrev_i32_e32 v5, 31, v4
	v_lshlrev_b64 v[4:5], 2, v[4:5]
	v_lshl_add_u64 v[8:9], s[6:7], 0, v[4:5]
	v_lshl_add_u64 v[4:5], s[8:9], 0, v[4:5]
	v_add_u32_e32 v4, s19, v70
	v_ashrrev_i32_e32 v5, 31, v4
	v_lshlrev_b64 v[4:5], 2, v[4:5]
	v_lshl_add_u64 v[8:9], s[6:7], 0, v[4:5]
	v_lshl_add_u64 v[12:13], s[8:9], 0, v[4:5]
	ds_read_b64 v[4:5], v117
	v_add_u32_e32 v14, s18, v128
	v_add_u32_e32 v15, s18, v129
	v_add_u32_e32 v11, s18, v125
	v_add_u32_e32 v0, s19, v124
	s_nop 0
	v_ashrrev_i32_e32 v1, 31, v0
	v_lshlrev_b64 v[0:1], 2, v[0:1]
	v_lshl_add_u64 v[6:7], s[6:7], 0, v[0:1]
	v_lshl_add_u64 v[0:1], s[8:9], 0, v[0:1]
	v_add_u32_e32 v12, s18, v126
	v_add_u32_e32 v13, s18, v127
	v_or_b32_e32 v1, s19, v118
	v_add_u32_e32 v0, s19, v120
	v_lshlrev_b32_e32 v64, 1, v1
	v_ashrrev_i32_e32 v1, 31, v0
	v_lshl_add_u64 v[78:79], v[0:1], 2, s[10:11]
	v_add_u32_e32 v10, s18, v120
	v_lshl_add_u64 v[6:7], s[2:3], 0, v[64:65]
	v_mad_i64_i32 v[154:155], s[4:5], v10, s60, v[6:7]
	v_mad_i64_i32 v[156:157], s[4:5], v11, s60, v[6:7]
	v_mad_i64_i32 v[158:159], s[4:5], v12, s60, v[6:7]
	v_mad_i64_i32 v[108:109], s[4:5], v13, s60, v[6:7]
	v_mad_i64_i32 v[104:105], s[4:5], v14, s60, v[6:7]
	v_mad_i64_i32 v[102:103], s[4:5], v15, s60, v[6:7]
	v_mad_i64_i32 v[100:101], s[4:5], v20, s60, v[6:7]
	v_mad_i64_i32 v[94:95], s[4:5], v21, s60, v[6:7]
	v_mad_i64_i32 v[92:93], s[4:5], v22, s60, v[6:7]
	v_mad_i64_i32 v[90:91], s[4:5], v23, s60, v[6:7]
	v_mad_i64_i32 v[88:89], s[4:5], v24, s60, v[6:7]
	v_mad_i64_i32 v[86:87], s[4:5], v25, s60, v[6:7]
	v_mad_i64_i32 v[84:85], s[4:5], v26, s60, v[6:7]
	v_mad_i64_i32 v[82:83], s[4:5], v27, s60, v[6:7]
	v_mad_i64_i32 v[80:81], s[4:5], v28, s60, v[6:7]
	v_mad_i64_i32 v[76:77], s[4:5], v29, s60, v[6:7]
	v_lshl_add_u64 v[74:75], s[0:1], 0, v[64:65]
	s_waitcnt lgkmcnt(0)
	s_barrier
; #define LAS __attribute__((address_space(3)))
; __device__ __forceinline__ int crow(int r, int hi) { return (r & 3) + 8 * (r >> 2) + 4 * hi; }
; template <int PH, bool PRB = false>
; __device__ __forceinline__ void run_phase(int layer, LAS unsigned char* lds, const int wv_) {
;     ...
;             f32x16 acc0, acc1;
; #pragma unroll
;             for (int r = 0; r < 16; ++r) { acc0[r] = 0.f; acc1[r] = 0.f; }
; #pragma unroll
;             for (int ks = 0; ks < 8; ++ks) {
;                 const bf16x8 b0 = *(const LAS bf16x8*)(vnt + (32 * cb0 + r32) * 272 + (16 * ks + 8 * hi) * 2);
;                 const bf16x8 b1 = *(const LAS bf16x8*)(vnt + (32 * (cb0 + 1) + r32) * 272 + (16 * ks + 8 * hi) * 2);
;                 acc0 = __builtin_amdgcn_mfma_f32_32x32x16_bf16(af[ks], b0, acc0, 0, 0, 0);
;                 acc1 = __builtin_amdgcn_mfma_f32_32x32x16_bf16(af[ks], b1, acc1, 0, 0, 0);
;             }
;             {
;                 const int col = g * 128 + 32 * cb0 + r32; bf16 u0[16], u1[16]; float bias[16];
; #pragma unroll
;                 for (int r = 0; r < 16; ++r) { const int prow = 32 * pb + att::crow(r, hi), tok = t0 + prow; bias[r] = bs[g * 128 + prow];
;                     u0[r] = z[(size_t)tok * EVEN_IN + col]; u1[r] = z[(size_t)tok * EVEN_IN + col + 32]; }
	ds_read_b128 v[0:3], v149
	ds_read_b128 v[96:99], v149 offset:32
	s_waitcnt lgkmcnt(1)
	v_mfma_f32_32x32x16_bf16 v[0:15], v[16:19], v[0:3], 0
	ds_read_b128 v[20:23], v149 offset:8704
	ds_read_b128 v[150:153], v149 offset:96
	s_waitcnt lgkmcnt(2)
	v_mfma_f32_32x32x16_bf16 v[0:15], v[56:59], v[96:99], v[0:15]
	ds_read_b128 v[96:99], v149 offset:8736
	s_waitcnt lgkmcnt(2)
	v_mfma_f32_32x32x16_bf16 v[16:31], v[16:19], v[20:23], 0
	s_waitcnt lgkmcnt(0)
	v_mfma_f32_32x32x16_bf16 v[16:31], v[56:59], v[96:99], v[16:31]
	ds_read_b128 v[96:99], v149 offset:64
	v_lshl_add_u64 v[56:57], v[74:75], 0, v[180:181]
	v_lshlrev_b64 v[180:181], 11, v[110:111]
	v_lshlrev_b64 v[110:111], 11, v[160:161]
	v_lshlrev_b64 v[58:59], 11, v[162:163]
	s_waitcnt lgkmcnt(0)
	v_mfma_f32_32x32x16_bf16 v[0:15], v[52:55], v[96:99], v[0:15]
	ds_read_b128 v[96:99], v149 offset:8768
	s_waitcnt lgkmcnt(0)
	v_mfma_f32_32x32x16_bf16 v[16:31], v[52:55], v[96:99], v[16:31]
	global_load_ushort v64, v[154:155], off
	global_load_dwordx4 v[52:55], v[78:79], off
	global_load_ushort v160, v[154:155], off offset:64
	global_load_ushort v161, v[156:157], off
	global_load_ushort v162, v[156:157], off offset:64
	global_load_ushort v163, v[158:159], off
	v_lshlrev_b64 v[96:97], 11, v[164:165]
	v_lshlrev_b64 v[98:99], 11, v[166:167]
	global_load_ushort v164, v[158:159], off offset:64
	v_mfma_f32_32x32x16_bf16 v[0:15], v[48:51], v[150:153], v[0:15]
	ds_read_b128 v[150:153], v149 offset:8800
	global_load_ushort v165, v[108:109], off
	global_load_ushort v166, v[108:109], off offset:64
	v_lshlrev_b64 v[154:155], 11, v[170:171]
	v_lshlrev_b64 v[156:157], 11, v[172:173]
	v_lshlrev_b64 v[108:109], 11, v[174:175]
	v_lshlrev_b64 v[158:159], 11, v[178:179]
	s_waitcnt lgkmcnt(0)
	v_mfma_f32_32x32x16_bf16 v[16:31], v[48:51], v[150:153], v[16:31]
	ds_read_b128 v[150:153], v149 offset:128
	global_load_ushort v167, v[104:105], off
	global_load_dwordx4 v[48:51], v[78:79], off offset:32
	global_load_ushort v168, v[104:105], off offset:64
	global_load_ushort v169, v[102:103], off
	global_load_ushort v170, v[102:103], off offset:64
	global_load_ushort v171, v[100:101], off
	global_load_ushort v172, v[100:101], off offset:64
	v_lshlrev_b64 v[104:105], 11, v[176:177]
	s_waitcnt lgkmcnt(0)
	v_mfma_f32_32x32x16_bf16 v[0:15], v[44:47], v[150:153], v[0:15]
	ds_read_b128 v[150:153], v149 offset:8832
	s_waitcnt lgkmcnt(0)
	v_mfma_f32_32x32x16_bf16 v[16:31], v[44:47], v[150:153], v[16:31]
	global_load_ushort v150, v[94:95], off
	global_load_ushort v151, v[94:95], off offset:64
	ds_read_b128 v[44:47], v149 offset:160
	v_lshlrev_b64 v[94:95], 11, v[106:107]
	global_load_ushort v106, v[92:93], off
	global_load_dwordx4 v[100:103], v[78:79], off offset:64
	global_load_ushort v107, v[92:93], off offset:64
	global_load_ushort v152, v[90:91], off
	global_load_ushort v153, v[90:91], off offset:64
	global_load_ushort v173, v[88:89], off
	global_load_ushort v174, v[88:89], off offset:64
	s_waitcnt lgkmcnt(0)
	v_mfma_f32_32x32x16_bf16 v[0:15], v[40:43], v[44:47], v[0:15]
	ds_read_b128 v[44:47], v149 offset:8864
	global_load_ushort v175, v[86:87], off
	global_load_ushort v176, v[86:87], off offset:64
	v_lshl_add_u64 v[90:91], v[74:75], 0, v[180:181]
	v_lshl_add_u64 v[92:93], v[74:75], 0, v[182:183]
	v_lshl_add_u64 v[86:87], v[74:75], 0, v[184:185]
	v_lshl_add_u64 v[88:89], v[74:75], 0, v[108:109]
	s_waitcnt lgkmcnt(0)
	v_mfma_f32_32x32x16_bf16 v[16:31], v[40:43], v[44:47], v[16:31]
	ds_read_b128 v[40:43], v149 offset:192
	global_load_ushort v177, v[84:85], off
	global_load_dwordx4 v[44:47], v[78:79], off offset:96
	global_load_ushort v178, v[84:85], off offset:64
	global_load_ushort v179, v[82:83], off
	global_load_ushort v180, v[82:83], off offset:64
	global_load_ushort v181, v[80:81], off
	v_lshl_add_u64 v[82:83], v[74:75], 0, v[110:111]
	global_load_ushort v110, v[80:81], off offset:64
	global_load_ushort v111, v[76:77], off
	global_load_ushort v182, v[76:77], off offset:64
	s_waitcnt lgkmcnt(0)
	v_mfma_f32_32x32x16_bf16 v[0:15], v[36:39], v[40:43], v[0:15]
	ds_read_b128 v[40:43], v149 offset:8896
	v_lshl_add_u64 v[78:79], v[74:75], 0, v[186:187]
	v_lshl_add_u64 v[76:77], v[74:75], 0, v[112:113]
	v_lshl_add_u64 v[80:81], v[74:75], 0, v[154:155]
	v_lshl_add_u64 v[84:85], v[74:75], 0, v[156:157]
	s_waitcnt vmcnt(2)
	v_lshlrev_b32_e32 v108, 16, v110
	s_waitcnt lgkmcnt(0)
	v_mfma_f32_32x32x16_bf16 v[16:31], v[36:39], v[40:43], v[16:31]
	ds_read_b128 v[36:39], v149 offset:224
	v_lshl_add_u64 v[40:41], v[74:75], 0, v[58:59]
	v_lshl_add_u64 v[42:43], v[74:75], 0, v[96:97]
	v_lshl_add_u64 v[58:59], v[74:75], 0, v[98:99]
	v_lshl_add_u64 v[96:97], v[74:75], 0, v[104:105]
	v_lshl_add_u64 v[98:99], v[74:75], 0, v[158:159]
	v_lshl_add_u64 v[74:75], v[74:75], 0, v[94:95]
	s_waitcnt lgkmcnt(0)
	v_mfma_f32_32x32x16_bf16 v[0:15], v[32:35], v[36:39], v[0:15]
	ds_read_b128 v[36:39], v149 offset:8928
	v_lshlrev_b32_e32 v94, 16, v107
	v_lshlrev_b32_e32 v95, 16, v152
	v_lshlrev_b32_e32 v104, 16, v174
	v_lshlrev_b32_e32 v105, 16, v176
	v_lshlrev_b32_e32 v107, 16, v180
	s_waitcnt vmcnt(0)
	v_lshlrev_b32_e32 v109, 16, v182
	s_waitcnt lgkmcnt(0)
; __device__ __forceinline__ float bf2f(bf16 b) { return __uint_as_float(((unsigned)b) << 16); }
; __device__ __forceinline__ bf16 f2bf(float f) { return (bf16)cvt_pk_bf16(f, f); }
; __device__ __forceinline__ int crow(int r, int hi) { return (r & 3) + 8 * (r >> 2) + 4 * hi; }
; template <int PH, bool PRB = false>
; __device__ __forceinline__ void run_phase(int layer, LAS unsigned char* lds, const int wv_) {
;     ...
;                 const int col = g * 128 + 32 * cb0 + r32; bf16 u0[16], u1[16]; float bias[16];
; #pragma unroll
;                 for (int r = 0; r < 16; ++r) { const int prow = 32 * pb + att::crow(r, hi), tok = t0 + prow; bias[r] = bs[g * 128 + prow];
;                     u0[r] = z[(size_t)tok * EVEN_IN + col]; u1[r] = z[(size_t)tok * EVEN_IN + col + 32]; }
; #pragma unroll
;                 for (int r = 0; r < 16; ++r) { const int tok = t0 + 32 * pb + att::crow(r, hi);
;                     y[(size_t)tok * D + col] = f2bf(bf2f(u0[r]) * (acc0[r] + bias[r]));
;                     y[(size_t)tok * D + col + 32] = f2bf(bf2f(u1[r]) * (acc1[r] + bias[r])); }
;             }
;             __syncthreads();
	v_mfma_f32_32x32x16_bf16 v[16:31], v[32:35], v[36:39], v[16:31]
	v_lshlrev_b32_e32 v32, 16, v64
	s_nop 0
	v_add_f32_e32 v0, v0, v52
	v_mul_f32_e32 v0, v0, v32
	v_lshlrev_b32_e32 v33, 16, v160
	v_cvt_pk_bf16_f32 v0, v0, v0
	v_lshlrev_b32_e32 v34, 16, v161
	v_add_f32_e32 v1, v1, v53
	s_nop 4
	v_add_f32_e32 v16, v52, v16
	v_mul_f32_e32 v16, v16, v33
	global_store_short v[56:57], v0, off
	v_cvt_pk_bf16_f32 v0, v16, v16
	v_lshlrev_b32_e32 v35, 16, v162
	v_add_f32_e32 v17, v53, v17
	v_mul_f32_e32 v1, v1, v34
	global_store_short v[56:57], v0, off offset:64
	v_cvt_pk_bf16_f32 v0, v1, v1
	v_lshlrev_b32_e32 v36, 16, v163
	v_add_f32_e32 v2, v2, v54
	v_mul_f32_e32 v17, v17, v35
	global_store_short v[90:91], v0, off
	v_cvt_pk_bf16_f32 v0, v17, v17
	v_lshlrev_b32_e32 v37, 16, v164
	v_add_f32_e32 v18, v54, v18
	v_mul_f32_e32 v2, v2, v36
	global_store_short v[90:91], v0, off offset:64
	v_cvt_pk_bf16_f32 v0, v2, v2
	v_lshlrev_b32_e32 v38, 16, v165
	v_add_f32_e32 v3, v3, v55
	v_mul_f32_e32 v18, v18, v37
	global_store_short v[92:93], v0, off
	v_cvt_pk_bf16_f32 v0, v18, v18
	v_lshlrev_b32_e32 v39, 16, v166
	v_add_f32_e32 v19, v55, v19
	v_mul_f32_e32 v3, v3, v38
	global_store_short v[92:93], v0, off offset:64
	v_cvt_pk_bf16_f32 v0, v3, v3
	v_lshlrev_b32_e32 v52, 16, v167
	v_add_f32_e32 v4, v4, v48
	v_mul_f32_e32 v19, v19, v39
	global_store_short v[86:87], v0, off
	v_cvt_pk_bf16_f32 v0, v19, v19
	v_lshlrev_b32_e32 v53, 16, v168
	v_add_f32_e32 v20, v48, v20
	v_mul_f32_e32 v4, v4, v52
	global_store_short v[86:87], v0, off offset:64
	v_cvt_pk_bf16_f32 v0, v4, v4
	v_lshlrev_b32_e32 v48, 16, v169
	v_add_f32_e32 v5, v5, v49
	v_mul_f32_e32 v20, v20, v53
	global_store_short v[78:79], v0, off
	v_cvt_pk_bf16_f32 v0, v20, v20
	v_lshlrev_b32_e32 v54, 16, v170
	v_add_f32_e32 v21, v49, v21
	v_mul_f32_e32 v5, v5, v48
	global_store_short v[78:79], v0, off offset:64
	v_cvt_pk_bf16_f32 v0, v5, v5
	v_lshlrev_b32_e32 v49, 16, v171
	v_add_f32_e32 v6, v6, v50
	v_mul_f32_e32 v21, v21, v54
	global_store_short v[82:83], v0, off
	v_cvt_pk_bf16_f32 v0, v21, v21
	v_lshlrev_b32_e32 v55, 16, v172
	v_add_f32_e32 v22, v50, v22
	v_mul_f32_e32 v6, v6, v49
	global_store_short v[82:83], v0, off offset:64
	v_cvt_pk_bf16_f32 v0, v6, v6
	v_lshlrev_b32_e32 v50, 16, v150
	v_add_f32_e32 v7, v7, v51
	v_mul_f32_e32 v22, v22, v55
	global_store_short v[40:41], v0, off
	v_cvt_pk_bf16_f32 v0, v22, v22
	v_lshlrev_b32_e32 v64, 16, v151
	v_add_f32_e32 v23, v51, v23
	v_mul_f32_e32 v7, v7, v50
	global_store_short v[40:41], v0, off offset:64
	v_cvt_pk_bf16_f32 v0, v7, v7
	v_lshlrev_b32_e32 v51, 16, v106
	v_add_f32_e32 v8, v8, v100
	v_mul_f32_e32 v23, v23, v64
	global_store_short v[42:43], v0, off
	v_cvt_pk_bf16_f32 v0, v23, v23
	v_add_f32_e32 v24, v100, v24
	v_mul_f32_e32 v8, v8, v51
	global_store_short v[42:43], v0, off offset:64
	v_cvt_pk_bf16_f32 v0, v8, v8
	v_add_f32_e32 v9, v9, v101
	v_mul_f32_e32 v24, v24, v94
	global_store_short v[58:59], v0, off
	v_cvt_pk_bf16_f32 v0, v24, v24
	v_lshlrev_b32_e32 v100, 16, v153
	v_add_f32_e32 v25, v101, v25
	v_mul_f32_e32 v9, v9, v95
	global_store_short v[58:59], v0, off offset:64
	v_cvt_pk_bf16_f32 v0, v9, v9
	v_lshlrev_b32_e32 v101, 16, v173
	v_add_f32_e32 v10, v10, v102
	v_mul_f32_e32 v25, v25, v100
	global_store_short v[76:77], v0, off
	v_cvt_pk_bf16_f32 v0, v25, v25
	v_add_f32_e32 v26, v102, v26
	v_mul_f32_e32 v10, v10, v101
	global_store_short v[76:77], v0, off offset:64
	v_cvt_pk_bf16_f32 v0, v10, v10
	v_lshlrev_b32_e32 v102, 16, v175
	v_add_f32_e32 v11, v11, v103
	v_mul_f32_e32 v26, v26, v104
	global_store_short v[80:81], v0, off
	v_cvt_pk_bf16_f32 v0, v26, v26
	v_add_f32_e32 v27, v103, v27
	v_mul_f32_e32 v11, v11, v102
	global_store_short v[80:81], v0, off offset:64
	v_cvt_pk_bf16_f32 v0, v11, v11
	v_lshlrev_b32_e32 v103, 16, v177
	v_add_f32_e32 v12, v12, v44
	v_mul_f32_e32 v27, v27, v105
	global_store_short v[84:85], v0, off
	v_cvt_pk_bf16_f32 v0, v27, v27
	v_lshlrev_b32_e32 v106, 16, v178
	v_add_f32_e32 v28, v44, v28
	v_mul_f32_e32 v12, v12, v103
	global_store_short v[84:85], v0, off offset:64
	v_cvt_pk_bf16_f32 v0, v12, v12
	v_lshlrev_b32_e32 v44, 16, v179
	v_add_f32_e32 v13, v13, v45
	v_mul_f32_e32 v28, v28, v106
	global_store_short v[88:89], v0, off
	v_cvt_pk_bf16_f32 v0, v28, v28
	v_add_f32_e32 v29, v45, v29
	v_mul_f32_e32 v13, v13, v44
	global_store_short v[88:89], v0, off offset:64
	v_cvt_pk_bf16_f32 v0, v13, v13
	v_lshlrev_b32_e32 v45, 16, v181
	v_add_f32_e32 v14, v14, v46
	v_mul_f32_e32 v29, v29, v107
	global_store_short v[96:97], v0, off
	v_cvt_pk_bf16_f32 v0, v29, v29
	v_add_f32_e32 v30, v46, v30
	v_mul_f32_e32 v14, v14, v45
	global_store_short v[96:97], v0, off offset:64
	v_cvt_pk_bf16_f32 v0, v14, v14
	v_lshlrev_b32_e32 v46, 16, v111
	v_add_f32_e32 v15, v15, v47
	v_mul_f32_e32 v30, v30, v108
	global_store_short v[98:99], v0, off
	v_cvt_pk_bf16_f32 v0, v30, v30
	v_add_f32_e32 v31, v47, v31
	v_mul_f32_e32 v15, v15, v46
	global_store_short v[98:99], v0, off offset:64
	v_cvt_pk_bf16_f32 v0, v15, v15
	v_mul_f32_e32 v31, v31, v109
	global_store_short v[74:75], v0, off
	v_cvt_pk_bf16_f32 v0, v31, v31
	global_store_short v[74:75], v0, off offset:64
	s_barrier
	s_cbranch_scc0 .LBB0_642
; template <int PH, bool PRB = false>
; __device__ __forceinline__ void run_phase(int layer, LAS unsigned char* lds, const int wv_) {
;     ...
;             const int pb = wid >> 1, cb0 = (wid & 1) * 2;
;             bf16x8 af[8];
; #pragma unroll
;             for (int ks = 0; ks < 8; ++ks) af[ks] = *(const bf16x8*)(sgw + (size_t)(g * 128 + 32 * pb + r32) * 128 + 16 * ks + 8 * hi);
;             {
;                 const int q = tid >> 2, part = tid & 3; const bf16* vp = z + (size_t)(t0 + q) * EVEN_IN + 512 + part * 128; float s = 0.f, s2 = 0.f;
; #pragma unroll
;                 for (int i = 0; i < 16; ++i) { const u32x4 w = *(const u32x4*)(vp + 8 * i);
; #pragma unroll
;                     for (int k = 0; k < 4; ++k) { const float a = __uint_as_float(w[k] << 16), b = __uint_as_float(w[k] & 0xffff0000u); s += a + b; s2 += a * a + b * b; } }
;                 s = xor_add<1>(s); s = xor_add<2>(s); s2 = xor_add<1>(s2); s2 = xor_add<2>(s2);
;                 const float mu = s * (1.f / 512.f), var = s2 * (1.f / 512.f) - mu * mu;
;                 if (part == 0) { st[2 * q] = mu; st[2 * q + 1] = rsqrtf(fmaxf(var, 0.f) + 1e-6f); }
;             }
;     ...
;             for (int it = 0; it < 4; ++it) { const int item = tid + NT * it; vw[it] = *(const u32x4*)(z + (size_t)(t0 + (item & 127)) * EVEN_IN + 512 + g * 128 + 8 * (item >> 7)); }
.LBB0_640:
	s_and_b32 s18, s17, 0xffffff80
	v_add_u32_e32 v0, s18, v115
	v_mad_i64_i32 v[28:29], s[4:5], v0, s60, v[72:73]
	global_load_dwordx4 v[8:11], v[28:29], off offset:1024
	global_load_dwordx4 v[20:23], v[28:29], off offset:1040
	global_load_dwordx4 v[24:27], v[28:29], off offset:1056
	global_load_dwordx4 v[74:77], v[28:29], off offset:1072
	s_and_b32 s19, s16, 0x180
	v_add_u32_e32 v0, s19, v114
	v_ashrrev_i32_e32 v1, 31, v0
	v_lshlrev_b64 v[16:17], 8, v[0:1]
	global_load_dwordx4 v[0:3], v[28:29], off offset:1136
	global_load_dwordx4 v[12:15], v[28:29], off offset:1120
	global_load_dwordx4 v[4:7], v[28:29], off offset:1104
	global_load_dwordx4 v[78:81], v[28:29], off offset:1088
	global_load_dwordx4 v[188:191], v[28:29], off offset:1168
	global_load_dwordx4 v[192:195], v[28:29], off offset:1152
	global_load_dwordx4 v[196:199], v[28:29], off offset:1200
	global_load_dwordx4 v[200:203], v[28:29], off offset:1184
	global_load_dwordx4 v[204:207], v[28:29], off offset:1232
	global_load_dwordx4 v[208:211], v[28:29], off offset:1216
	global_load_dwordx4 v[212:215], v[28:29], off offset:1264
	global_load_dwordx4 v[222:225], v[28:29], off offset:1248
	v_lshl_add_u64 v[30:31], v[60:61], 0, v[16:17]
	global_load_dwordx4 v[16:19], v[30:31], off
	global_load_dwordx4 v[56:59], v[30:31], off offset:32
	global_load_dwordx4 v[52:55], v[30:31], off offset:64
	global_load_dwordx4 v[48:51], v[30:31], off offset:96
	global_load_dwordx4 v[44:47], v[30:31], off offset:128
	global_load_dwordx4 v[40:43], v[30:31], off offset:160
	global_load_dwordx4 v[36:39], v[30:31], off offset:192
	global_load_dwordx4 v[32:35], v[30:31], off offset:224
	v_or_b32_e32 v250, s18, v116
	v_mov_b64_e32 v[252:253], s[2:3]
	v_mad_i64_i32 v[252:253], s[4:5], v250, s60, v[252:253]
	s_lshl_b32 s50, s19, 1
	v_lshl_add_u64 v[252:253], v[252:253], 0, s[50:51]
	v_lshl_add_u64 v[250:251], v[62:63], 1, v[252:253]
	global_load_dwordx4 v[230:233], v[250:251], off offset:1024
	v_lshl_add_u64 v[250:251], v[66:67], 1, v[252:253]
	global_load_dwordx4 v[234:237], v[250:251], off offset:1024
	v_lshl_add_u64 v[250:251], v[68:69], 1, v[252:253]
	global_load_dwordx4 v[238:241], v[250:251], off offset:1024
	v_lshl_add_u64 v[250:251], v[70:71], 1, v[252:253]
	global_load_dwordx4 v[246:249], v[250:251], off offset:1024
	s_waitcnt vmcnt(27)
	v_and_b32_e32 v83, 0xffff0000, v9
	v_lshlrev_b32_e32 v9, 16, v9
	v_and_b32_e32 v31, 0xffff0000, v8
	v_lshlrev_b32_e32 v8, 16, v8
	v_mov_b32_e32 v30, v9
	v_mul_f32_e32 v150, v8, v8
	v_pk_add_f32 v[152:153], v[8:9], v[30:31] op_sel:[1,0] op_sel_hi:[0,1]
	v_mov_b32_e32 v151, v9
	v_pk_mul_f32 v[8:9], v[8:9], v[30:31] op_sel:[1,0] op_sel_hi:[0,1]
	v_lshlrev_b32_e32 v85, 16, v10
	v_and_b32_e32 v87, 0xffff0000, v10
	v_mul_f32_e32 v64, v83, v83
	v_mul_f32_e32 v82, v31, v31
	v_mov_b32_e32 v9, v153
	v_lshlrev_b32_e32 v89, 16, v11
	v_and_b32_e32 v11, 0xffff0000, v11
	v_mul_f32_e32 v84, v85, v85
	v_mul_f32_e32 v86, v87, v87
	v_pk_add_f32 v[30:31], v[150:151], v[82:83]
	v_pk_add_f32 v[8:9], v[8:9], v[64:65]
	s_waitcnt vmcnt(26)
	v_lshlrev_b32_e32 v91, 16, v20
	v_and_b32_e32 v93, 0xffff0000, v20
	v_mul_f32_e32 v88, v89, v89
	v_mul_f32_e32 v10, v11, v11
	v_pk_add_f32 v[82:83], v[84:85], v[86:87]
	v_pk_add_f32 v[8:9], v[30:31], v[8:9]
	v_lshlrev_b32_e32 v95, 16, v21
	v_and_b32_e32 v21, 0xffff0000, v21
	v_mul_f32_e32 v90, v91, v91
	v_mul_f32_e32 v92, v93, v93
	v_pk_add_f32 v[10:11], v[88:89], v[10:11]
	v_pk_add_f32 v[8:9], v[82:83], v[8:9]
	v_lshlrev_b32_e32 v97, 16, v22
	v_and_b32_e32 v99, 0xffff0000, v22
	v_mul_f32_e32 v94, v95, v95
	v_mul_f32_e32 v20, v21, v21
	v_pk_add_f32 v[84:85], v[90:91], v[92:93]
	v_pk_add_f32 v[8:9], v[10:11], v[8:9]
	v_lshlrev_b32_e32 v101, 16, v23
	v_and_b32_e32 v23, 0xffff0000, v23
	v_mul_f32_e32 v96, v97, v97
	v_mul_f32_e32 v98, v99, v99
	v_pk_add_f32 v[20:21], v[94:95], v[20:21]
	v_pk_add_f32 v[8:9], v[84:85], v[8:9]
	s_waitcnt vmcnt(25)
	v_lshlrev_b32_e32 v103, 16, v24
	v_and_b32_e32 v105, 0xffff0000, v24
	v_mul_f32_e32 v100, v101, v101
	v_mul_f32_e32 v22, v23, v23
	v_pk_add_f32 v[86:87], v[96:97], v[98:99]
	v_pk_add_f32 v[8:9], v[20:21], v[8:9]
	v_lshlrev_b32_e32 v107, 16, v25
	v_and_b32_e32 v25, 0xffff0000, v25
	v_mul_f32_e32 v102, v103, v103
	v_mul_f32_e32 v104, v105, v105
	v_pk_add_f32 v[22:23], v[100:101], v[22:23]
	v_pk_add_f32 v[8:9], v[86:87], v[8:9]
	v_lshlrev_b32_e32 v109, 16, v26
	v_and_b32_e32 v111, 0xffff0000, v26
	v_mul_f32_e32 v106, v107, v107
	v_mul_f32_e32 v24, v25, v25
	v_pk_add_f32 v[88:89], v[102:103], v[104:105]
	v_pk_add_f32 v[8:9], v[22:23], v[8:9]
	v_mul_f32_e32 v108, v109, v109
	v_mul_f32_e32 v110, v111, v111
	v_pk_add_f32 v[24:25], v[106:107], v[24:25]
	v_pk_add_f32 v[8:9], v[88:89], v[8:9]
	v_pk_add_f32 v[90:91], v[108:109], v[110:111]
	v_pk_add_f32 v[8:9], v[24:25], v[8:9]
	v_lshlrev_b32_e32 v113, 16, v27
	v_pk_add_f32 v[24:25], v[90:91], v[8:9]
	s_waitcnt vmcnt(18)
	v_mov_b64_e32 v[8:9], v[188:189]
	v_mov_b64_e32 v[10:11], v[190:191]
	v_mov_b64_e32 v[20:21], v[192:193]
	v_mov_b64_e32 v[22:23], v[194:195]
	v_and_b32_e32 v27, 0xffff0000, v27
	v_mul_f32_e32 v112, v113, v113
	v_mul_f32_e32 v26, v27, v27
	s_waitcnt vmcnt(18)
	v_lshlrev_b32_e32 v31, 16, v74
	v_and_b32_e32 v83, 0xffff0000, v74
	v_pk_add_f32 v[26:27], v[112:113], v[26:27]
	v_mul_f32_e32 v30, v31, v31
	v_mul_f32_e32 v82, v83, v83
	v_lshlrev_b32_e32 v85, 16, v75
	v_and_b32_e32 v75, 0xffff0000, v75
	v_mul_f32_e32 v84, v85, v85
	v_mul_f32_e32 v74, v75, v75
	v_lshlrev_b32_e32 v87, 16, v76
	v_and_b32_e32 v89, 0xffff0000, v76
	v_pk_add_f32 v[24:25], v[26:27], v[24:25]
	v_pk_add_f32 v[26:27], v[30:31], v[82:83]
	v_mul_f32_e32 v86, v87, v87
	v_mul_f32_e32 v88, v89, v89
	v_lshlrev_b32_e32 v91, 16, v77
	v_and_b32_e32 v77, 0xffff0000, v77
	v_pk_add_f32 v[24:25], v[26:27], v[24:25]
	v_pk_add_f32 v[26:27], v[84:85], v[74:75]
	v_mul_f32_e32 v90, v91, v91
	v_mul_f32_e32 v76, v77, v77
	s_waitcnt vmcnt(18)
; template <int PH, bool PRB = false>
; __device__ __forceinline__ void run_phase(int layer, LAS unsigned char* lds, const int wv_) {
;     ...
;                 const int q = tid >> 2, part = tid & 3; const bf16* vp = z + (size_t)(t0 + q) * EVEN_IN + 512 + part * 128; float s = 0.f, s2 = 0.f;
; #pragma unroll
;                 for (int i = 0; i < 16; ++i) { const u32x4 w = *(const u32x4*)(vp + 8 * i);
; #pragma unroll
;                     for (int k = 0; k < 4; ++k) { const float a = __uint_as_float(w[k] << 16), b = __uint_as_float(w[k] & 0xffff0000u); s += a + b; s2 += a * a + b * b; } }
	v_lshlrev_b32_e32 v93, 16, v78
	v_and_b32_e32 v95, 0xffff0000, v78
	v_pk_add_f32 v[24:25], v[26:27], v[24:25]
	v_pk_add_f32 v[26:27], v[86:87], v[88:89]
	v_mul_f32_e32 v92, v93, v93
	v_mul_f32_e32 v94, v95, v95
	v_lshlrev_b32_e32 v97, 16, v79
	v_and_b32_e32 v79, 0xffff0000, v79
	v_pk_add_f32 v[24:25], v[26:27], v[24:25]
	v_pk_add_f32 v[26:27], v[90:91], v[76:77]
	v_mul_f32_e32 v96, v97, v97
	v_mul_f32_e32 v78, v79, v79
	v_lshlrev_b32_e32 v99, 16, v80
	v_and_b32_e32 v101, 0xffff0000, v80
	v_pk_add_f32 v[24:25], v[26:27], v[24:25]
	v_pk_add_f32 v[26:27], v[92:93], v[94:95]
	v_mul_f32_e32 v98, v99, v99
	v_mul_f32_e32 v100, v101, v101
	v_lshlrev_b32_e32 v103, 16, v81
	v_and_b32_e32 v81, 0xffff0000, v81
	v_pk_add_f32 v[24:25], v[26:27], v[24:25]
	v_pk_add_f32 v[26:27], v[96:97], v[78:79]
	v_mul_f32_e32 v102, v103, v103
	v_mul_f32_e32 v80, v81, v81
	v_lshlrev_b32_e32 v105, 16, v4
	v_and_b32_e32 v107, 0xffff0000, v4
	v_pk_add_f32 v[24:25], v[26:27], v[24:25]
	v_pk_add_f32 v[26:27], v[98:99], v[100:101]
	v_mul_f32_e32 v104, v105, v105
	v_mul_f32_e32 v106, v107, v107
	v_lshlrev_b32_e32 v109, 16, v5
	v_and_b32_e32 v5, 0xffff0000, v5
	v_pk_add_f32 v[24:25], v[26:27], v[24:25]
	v_pk_add_f32 v[26:27], v[102:103], v[80:81]
	v_mul_f32_e32 v108, v109, v109
	v_mul_f32_e32 v4, v5, v5
	v_pk_add_f32 v[24:25], v[26:27], v[24:25]
	v_pk_add_f32 v[26:27], v[104:105], v[106:107]
	v_pk_add_f32 v[4:5], v[108:109], v[4:5]
	v_pk_add_f32 v[24:25], v[26:27], v[24:25]
	v_lshlrev_b32_e32 v77, 16, v7
	v_pk_add_f32 v[30:31], v[4:5], v[24:25]
	v_lshlrev_b32_e32 v5, 16, v6
	v_and_b32_e32 v25, 0xffff0000, v6
	v_mul_f32_e32 v4, v5, v5
	v_mul_f32_e32 v24, v25, v25
	v_and_b32_e32 v79, 0xffff0000, v7
	v_pk_add_f32 v[74:75], v[4:5], v[24:25]
	v_mul_f32_e32 v76, v77, v77
	v_mul_f32_e32 v78, v79, v79
	v_lshlrev_b32_e32 v81, 16, v12
	v_and_b32_e32 v83, 0xffff0000, v12
	v_mul_f32_e32 v80, v81, v81
	v_mul_f32_e32 v82, v83, v83
	v_lshlrev_b32_e32 v85, 16, v13
	v_and_b32_e32 v13, 0xffff0000, v13
	v_pk_add_f32 v[30:31], v[74:75], v[30:31]
	v_pk_add_f32 v[74:75], v[76:77], v[78:79]
	v_mul_f32_e32 v84, v85, v85
	v_mul_f32_e32 v12, v13, v13
	v_lshlrev_b32_e32 v87, 16, v14
	s_waitcnt vmcnt(16)
	v_mov_b64_e32 v[4:5], v[196:197]
	v_mov_b64_e32 v[6:7], v[198:199]
	v_mov_b64_e32 v[24:25], v[200:201]
	v_mov_b64_e32 v[26:27], v[202:203]
	v_and_b32_e32 v89, 0xffff0000, v14
	v_pk_add_f32 v[30:31], v[74:75], v[30:31]
	v_pk_add_f32 v[74:75], v[80:81], v[82:83]
	v_mul_f32_e32 v86, v87, v87
	v_mul_f32_e32 v88, v89, v89
	v_lshlrev_b32_e32 v91, 16, v15
	v_and_b32_e32 v15, 0xffff0000, v15
	v_pk_add_f32 v[30:31], v[74:75], v[30:31]
	v_pk_add_f32 v[12:13], v[84:85], v[12:13]
	v_mul_f32_e32 v90, v91, v91
	v_mul_f32_e32 v14, v15, v15
	v_lshlrev_b32_e32 v93, 16, v0
	v_and_b32_e32 v95, 0xffff0000, v0
	v_pk_add_f32 v[12:13], v[12:13], v[30:31]
	v_pk_add_f32 v[30:31], v[86:87], v[88:89]
	v_mul_f32_e32 v92, v93, v93
	v_mul_f32_e32 v94, v95, v95
	v_lshlrev_b32_e32 v97, 16, v1
	v_and_b32_e32 v1, 0xffff0000, v1
	v_pk_add_f32 v[12:13], v[30:31], v[12:13]
	v_pk_add_f32 v[14:15], v[90:91], v[14:15]
	v_mul_f32_e32 v96, v97, v97
	v_mul_f32_e32 v0, v1, v1
	v_lshlrev_b32_e32 v99, 16, v2
	v_and_b32_e32 v101, 0xffff0000, v2
	v_pk_add_f32 v[12:13], v[14:15], v[12:13]
	v_pk_add_f32 v[14:15], v[92:93], v[94:95]
	v_mul_f32_e32 v98, v99, v99
	v_mul_f32_e32 v100, v101, v101
	v_lshlrev_b32_e32 v103, 16, v3
	v_and_b32_e32 v3, 0xffff0000, v3
	v_pk_add_f32 v[12:13], v[14:15], v[12:13]
	v_pk_add_f32 v[0:1], v[96:97], v[0:1]
	v_mul_f32_e32 v102, v103, v103
	v_mul_f32_e32 v2, v3, v3
	s_waitcnt vmcnt(16)
	v_lshlrev_b32_e32 v105, 16, v20
	v_and_b32_e32 v107, 0xffff0000, v20
	v_pk_add_f32 v[0:1], v[0:1], v[12:13]
	v_pk_add_f32 v[12:13], v[98:99], v[100:101]
	v_mul_f32_e32 v104, v105, v105
	v_mul_f32_e32 v106, v107, v107
	v_pk_add_f32 v[0:1], v[12:13], v[0:1]
	v_pk_add_f32 v[2:3], v[102:103], v[2:3]
	v_lshlrev_b32_e32 v75, 16, v22
	v_pk_add_f32 v[0:1], v[2:3], v[0:1]
	v_pk_add_f32 v[2:3], v[104:105], v[106:107]
	v_and_b32_e32 v77, 0xffff0000, v22
	v_pk_add_f32 v[30:31], v[2:3], v[0:1]
	v_lshlrev_b32_e32 v1, 16, v21
	v_and_b32_e32 v3, 0xffff0000, v21
	v_mul_f32_e32 v0, v1, v1
	v_mul_f32_e32 v2, v3, v3
	v_pk_add_f32 v[20:21], v[0:1], v[2:3]
	s_waitcnt vmcnt(14)
	v_mov_b64_e32 v[0:1], v[204:205]
	v_mov_b64_e32 v[2:3], v[206:207]
	v_mov_b64_e32 v[12:13], v[208:209]
	v_mov_b64_e32 v[14:15], v[210:211]
	v_mul_f32_e32 v74, v75, v75
	v_mul_f32_e32 v76, v77, v77
	v_lshlrev_b32_e32 v79, 16, v23
	v_and_b32_e32 v23, 0xffff0000, v23
	v_mul_f32_e32 v78, v79, v79
	v_mul_f32_e32 v22, v23, v23
	v_lshlrev_b32_e32 v81, 16, v8
	v_and_b32_e32 v83, 0xffff0000, v8
	v_pk_add_f32 v[20:21], v[20:21], v[30:31]
	v_pk_add_f32 v[30:31], v[74:75], v[76:77]
	v_mul_f32_e32 v80, v81, v81
	v_mul_f32_e32 v82, v83, v83
	v_lshlrev_b32_e32 v85, 16, v9
	v_and_b32_e32 v9, 0xffff0000, v9
	v_pk_add_f32 v[20:21], v[30:31], v[20:21]
	v_pk_add_f32 v[22:23], v[78:79], v[22:23]
	v_mul_f32_e32 v84, v85, v85
	v_mul_f32_e32 v8, v9, v9
	v_lshlrev_b32_e32 v87, 16, v10
	v_and_b32_e32 v89, 0xffff0000, v10
	v_pk_add_f32 v[20:21], v[22:23], v[20:21]
	v_pk_add_f32 v[22:23], v[80:81], v[82:83]
	v_mul_f32_e32 v86, v87, v87
	v_mul_f32_e32 v88, v89, v89
	v_lshlrev_b32_e32 v91, 16, v11
	v_and_b32_e32 v11, 0xffff0000, v11
	v_pk_add_f32 v[20:21], v[22:23], v[20:21]
	v_pk_add_f32 v[8:9], v[84:85], v[8:9]
	v_mul_f32_e32 v90, v91, v91
	v_mul_f32_e32 v10, v11, v11
	v_pk_add_f32 v[8:9], v[8:9], v[20:21]
	v_pk_add_f32 v[20:21], v[86:87], v[88:89]
	v_pk_add_f32 v[10:11], v[90:91], v[10:11]
	v_pk_add_f32 v[8:9], v[20:21], v[8:9]
	s_waitcnt vmcnt(14)
	v_lshlrev_b32_e32 v93, 16, v24
	v_pk_add_f32 v[30:31], v[10:11], v[8:9]
	s_waitcnt vmcnt(12)
; template <int PH, bool PRB = false>
; __device__ __forceinline__ void run_phase(int layer, LAS unsigned char* lds, const int wv_) {
;     ...
;                 const int q = tid >> 2, part = tid & 3; const bf16* vp = z + (size_t)(t0 + q) * EVEN_IN + 512 + part * 128; float s = 0.f, s2 = 0.f;
; #pragma unroll
;                 for (int i = 0; i < 16; ++i) { const u32x4 w = *(const u32x4*)(vp + 8 * i);
; #pragma unroll
;                     for (int k = 0; k < 4; ++k) { const float a = __uint_as_float(w[k] << 16), b = __uint_as_float(w[k] & 0xffff0000u); s += a + b; s2 += a * a + b * b; } }
;                 s = xor_add<1>(s); s = xor_add<2>(s); s2 = xor_add<1>(s2); s2 = xor_add<2>(s2);
;                 const float mu = s * (1.f / 512.f), var = s2 * (1.f / 512.f) - mu * mu;
;                 if (part == 0) { st[2 * q] = mu; st[2 * q + 1] = rsqrtf(fmaxf(var, 0.f) + 1e-6f); }
	v_mov_b64_e32 v[8:9], v[212:213]
	v_mov_b64_e32 v[10:11], v[214:215]
	v_mov_b64_e32 v[20:21], v[222:223]
	v_mov_b64_e32 v[22:23], v[224:225]
	v_and_b32_e32 v95, 0xffff0000, v24
	v_mul_f32_e32 v92, v93, v93
	v_mul_f32_e32 v94, v95, v95
	v_lshlrev_b32_e32 v97, 16, v25
	v_and_b32_e32 v25, 0xffff0000, v25
	v_mul_f32_e32 v96, v97, v97
	v_mul_f32_e32 v24, v25, v25
	v_lshlrev_b32_e32 v99, 16, v26
	v_and_b32_e32 v101, 0xffff0000, v26
	v_pk_add_f32 v[28:29], v[92:93], v[94:95]
	v_mul_f32_e32 v98, v99, v99
	v_mul_f32_e32 v100, v101, v101
	v_lshlrev_b32_e32 v103, 16, v27
	v_and_b32_e32 v27, 0xffff0000, v27
	v_pk_add_f32 v[28:29], v[28:29], v[30:31]
	v_pk_add_f32 v[24:25], v[96:97], v[24:25]
	v_mul_f32_e32 v102, v103, v103
	v_mul_f32_e32 v26, v27, v27
	v_pk_add_f32 v[24:25], v[24:25], v[28:29]
	v_pk_add_f32 v[28:29], v[98:99], v[100:101]
	v_pk_add_f32 v[26:27], v[102:103], v[26:27]
	v_pk_add_f32 v[24:25], v[28:29], v[24:25]
	v_and_b32_e32 v29, 0xffff0000, v4
	v_pk_add_f32 v[24:25], v[26:27], v[24:25]
	v_lshlrev_b32_e32 v27, 16, v4
	v_mul_f32_e32 v26, v27, v27
	v_mul_f32_e32 v28, v29, v29
	v_pk_add_f32 v[26:27], v[26:27], v[28:29]
	v_lshlrev_b32_e32 v29, 16, v5
	v_and_b32_e32 v5, 0xffff0000, v5
	v_mul_f32_e32 v28, v29, v29
	v_mul_f32_e32 v4, v5, v5
	v_lshlrev_b32_e32 v31, 16, v6
	v_and_b32_e32 v75, 0xffff0000, v6
	v_mul_f32_e32 v30, v31, v31
	v_mul_f32_e32 v74, v75, v75
	v_lshlrev_b32_e32 v77, 16, v7
	v_and_b32_e32 v7, 0xffff0000, v7
	v_pk_add_f32 v[24:25], v[26:27], v[24:25]
	v_pk_add_f32 v[4:5], v[28:29], v[4:5]
	v_mul_f32_e32 v76, v77, v77
	v_mul_f32_e32 v6, v7, v7
	s_waitcnt vmcnt(12)
	v_lshlrev_b32_e32 v79, 16, v12
	v_and_b32_e32 v81, 0xffff0000, v12
	v_pk_add_f32 v[4:5], v[4:5], v[24:25]
	v_pk_add_f32 v[24:25], v[30:31], v[74:75]
	v_mul_f32_e32 v78, v79, v79
	v_mul_f32_e32 v80, v81, v81
	v_lshlrev_b32_e32 v83, 16, v13
	v_and_b32_e32 v13, 0xffff0000, v13
	v_pk_add_f32 v[4:5], v[24:25], v[4:5]
	v_pk_add_f32 v[6:7], v[76:77], v[6:7]
	v_mul_f32_e32 v82, v83, v83
	v_mul_f32_e32 v12, v13, v13
	v_lshlrev_b32_e32 v85, 16, v14
	v_and_b32_e32 v87, 0xffff0000, v14
	v_pk_add_f32 v[4:5], v[6:7], v[4:5]
	v_pk_add_f32 v[6:7], v[78:79], v[80:81]
	v_mul_f32_e32 v84, v85, v85
	v_mul_f32_e32 v86, v87, v87
	v_lshlrev_b32_e32 v89, 16, v15
	v_and_b32_e32 v15, 0xffff0000, v15
	v_pk_add_f32 v[4:5], v[6:7], v[4:5]
	v_pk_add_f32 v[6:7], v[82:83], v[12:13]
	v_mul_f32_e32 v88, v89, v89
	v_mul_f32_e32 v14, v15, v15
	v_lshlrev_b32_e32 v91, 16, v0
	v_and_b32_e32 v93, 0xffff0000, v0
	v_pk_add_f32 v[4:5], v[6:7], v[4:5]
	v_pk_add_f32 v[6:7], v[84:85], v[86:87]
	v_mul_f32_e32 v90, v91, v91
	v_mul_f32_e32 v92, v93, v93
	v_lshlrev_b32_e32 v95, 16, v1
	v_and_b32_e32 v1, 0xffff0000, v1
	v_pk_add_f32 v[4:5], v[6:7], v[4:5]
	v_pk_add_f32 v[6:7], v[88:89], v[14:15]
	v_mul_f32_e32 v94, v95, v95
	v_mul_f32_e32 v0, v1, v1
	v_lshlrev_b32_e32 v97, 16, v2
	v_and_b32_e32 v99, 0xffff0000, v2
	v_pk_add_f32 v[4:5], v[6:7], v[4:5]
	v_pk_add_f32 v[6:7], v[90:91], v[92:93]
	v_mul_f32_e32 v96, v97, v97
	v_mul_f32_e32 v98, v99, v99
	v_pk_add_f32 v[4:5], v[6:7], v[4:5]
	v_pk_add_f32 v[0:1], v[94:95], v[0:1]
	s_waitcnt vmcnt(0)
	v_and_b32_e32 v7, 0xffff0000, v20
	v_pk_add_f32 v[0:1], v[0:1], v[4:5]
	v_pk_add_f32 v[4:5], v[96:97], v[98:99]
	v_mul_f32_e32 v6, v7, v7
	v_pk_add_f32 v[0:1], v[4:5], v[0:1]
	v_lshlrev_b32_e32 v5, 16, v3
	v_and_b32_e32 v3, 0xffff0000, v3
	v_mul_f32_e32 v4, v5, v5
	v_mul_f32_e32 v2, v3, v3
	v_pk_add_f32 v[2:3], v[4:5], v[2:3]
	v_lshlrev_b32_e32 v5, 16, v20
	v_mul_f32_e32 v4, v5, v5
	v_lshlrev_b32_e32 v13, 16, v21
	v_and_b32_e32 v15, 0xffff0000, v21
	v_mul_f32_e32 v12, v13, v13
	v_mul_f32_e32 v14, v15, v15
	v_lshlrev_b32_e32 v21, 16, v22
	v_and_b32_e32 v25, 0xffff0000, v22
	v_pk_add_f32 v[0:1], v[2:3], v[0:1]
	v_pk_add_f32 v[2:3], v[4:5], v[6:7]
	v_mul_f32_e32 v20, v21, v21
	v_mul_f32_e32 v24, v25, v25
	v_lshlrev_b32_e32 v27, 16, v23
	v_and_b32_e32 v23, 0xffff0000, v23
	v_pk_add_f32 v[0:1], v[2:3], v[0:1]
	v_pk_add_f32 v[2:3], v[12:13], v[14:15]
	v_mul_f32_e32 v26, v27, v27
	v_mul_f32_e32 v22, v23, v23
	v_lshlrev_b32_e32 v29, 16, v8
	v_and_b32_e32 v31, 0xffff0000, v8
	v_pk_add_f32 v[0:1], v[2:3], v[0:1]
	v_pk_add_f32 v[2:3], v[20:21], v[24:25]
	v_mul_f32_e32 v28, v29, v29
	v_mul_f32_e32 v30, v31, v31
	v_lshlrev_b32_e32 v75, 16, v9
	v_and_b32_e32 v9, 0xffff0000, v9
	v_pk_add_f32 v[0:1], v[2:3], v[0:1]
	v_pk_add_f32 v[2:3], v[26:27], v[22:23]
	v_mul_f32_e32 v74, v75, v75
	v_mul_f32_e32 v8, v9, v9
	v_lshlrev_b32_e32 v77, 16, v10
	v_and_b32_e32 v79, 0xffff0000, v10
	v_pk_add_f32 v[0:1], v[2:3], v[0:1]
	v_pk_add_f32 v[2:3], v[28:29], v[30:31]
	v_mul_f32_e32 v76, v77, v77
	v_mul_f32_e32 v78, v79, v79
	v_lshlrev_b32_e32 v81, 16, v11
	v_and_b32_e32 v11, 0xffff0000, v11
	v_pk_add_f32 v[0:1], v[2:3], v[0:1]
	v_pk_add_f32 v[2:3], v[74:75], v[8:9]
	v_mul_f32_e32 v80, v81, v81
	v_mul_f32_e32 v10, v11, v11
	v_pk_add_f32 v[0:1], v[2:3], v[0:1]
	v_pk_add_f32 v[2:3], v[76:77], v[78:79]
	s_nop 0
	v_pk_add_f32 v[0:1], v[2:3], v[0:1]
	v_pk_add_f32 v[2:3], v[80:81], v[10:11]
	s_nop 0
	v_pk_add_f32 v[0:1], v[2:3], v[0:1]
	ds_swizzle_b32 v3, v1 offset:swizzle(SWAP,1)
	ds_swizzle_b32 v2, v0 offset:swizzle(SWAP,1)
	s_waitcnt lgkmcnt(0)
	v_pk_add_f32 v[0:1], v[0:1], v[2:3]
	ds_swizzle_b32 v3, v1 offset:swizzle(SWAP,2)
	ds_swizzle_b32 v2, v0 offset:swizzle(SWAP,2)
	s_and_saveexec_b64 s[12:13], vcc
	s_cbranch_execz .LBB0_639
	s_waitcnt lgkmcnt(0)
	v_pk_add_f32 v[0:1], v[0:1], v[2:3]
	s_mov_b32 s4, 0x3b000000
	v_pk_mul_f32 v[0:1], v[0:1], s[4:5] op_sel_hi:[1,0]
	s_nop 0
	v_fma_f32 v0, -v1, v1, v0
	v_max_f32_e32 v0, 0, v0
	v_add_f32_e32 v0, 0x358637bd, v0
	v_mul_f32_e32 v2, 0x4b800000, v0
	v_cmp_gt_f32_e64 s[4:5], s61, v0
	s_nop 1
	v_cndmask_b32_e64 v0, v0, v2, s[4:5]
	v_rsq_f32_e32 v0, v0
	s_nop 0
	v_mul_f32_e32 v2, 0x45800000, v0
	v_cndmask_b32_e64 v3, v0, v2, s[4:5]
	v_mov_b32_e32 v2, v1
	ds_write_b64 v140, v[2:3]
	s_branch .LBB0_639
